# blocking MALL/L2 prefetch of phase weights at start of phases B,E,F,H,J
# baseline (speedup 1.0000x reference)
.LBB0_3295:
	v_readlane_b32 s2, v254, 0
	v_readlane_b32 s3, v254, 1
	s_load_dword s0, s[2:3], 0x128
	s_mul_i32 s4, s48, 13
	s_mov_b32 s49, s93
	s_add_i32 s69, s4, 2
	v_writelane_b32 v254, s48, 51
	s_waitcnt lgkmcnt(0)
	s_cmp_le_i32 s0, s69
	v_writelane_b32 v254, s49, 52
	s_cbranch_scc0 .LBB0_3540
	s_load_dword s0, s[2:3], 0x12c
	s_waitcnt lgkmcnt(0)
	s_cmp_ge_i32 s69, s0
	s_cbranch_scc1 .LBB0_3540
	v_readlane_b32 s12, v254, 0
	v_readlane_b32 s13, v254, 1
	s_load_dwordx2 s[72:73], s[12:13], 0x120
	v_lshlrev_b32_e32 v0, 4, v235
	s_waitcnt lgkmcnt(0)
	s_mul_i32 s12, s48, 0x1400000
	s_mul_i32 s13, s43, 0x14000
	s_add_u32 s12, s12, s13
	s_add_u32 s12, s12, 0x1100000
	s_add_u32 s54, s72, s12
	s_addc_u32 s55, s73, 0
	v_mov_b32_e32 v3, v0
	global_load_dwordx4 v[4:7], v3, s[54:55]
	v_add_u32_e32 v3, 0x2000, v3
	global_load_dwordx4 v[8:11], v3, s[54:55]
	v_add_u32_e32 v3, 0x2000, v3
	global_load_dwordx4 v[12:15], v3, s[54:55]
	v_add_u32_e32 v3, 0x2000, v3
	global_load_dwordx4 v[16:19], v3, s[54:55]
	v_add_u32_e32 v3, 0x2000, v3
	global_load_dwordx4 v[20:23], v3, s[54:55]
	v_add_u32_e32 v3, 0x2000, v3
	global_load_dwordx4 v[24:27], v3, s[54:55]
	v_add_u32_e32 v3, 0x2000, v3
	global_load_dwordx4 v[28:31], v3, s[54:55]
	v_add_u32_e32 v3, 0x2000, v3
	global_load_dwordx4 v[32:35], v3, s[54:55]
	v_add_u32_e32 v3, 0x2000, v3
	s_waitcnt vmcnt(0)
	global_load_dwordx4 v[4:7], v3, s[54:55]
	v_add_u32_e32 v3, 0x2000, v3
	global_load_dwordx4 v[8:11], v3, s[54:55]
	v_add_u32_e32 v3, 0x2000, v3
	s_waitcnt vmcnt(0)
	s_mul_i32 s12, s48, 0x400000
	s_mul_i32 s13, s43, 0x4000
	s_add_u32 s12, s12, s13
	s_add_u32 s12, s12, 0x100000
	s_add_u32 s54, s72, s12
	s_addc_u32 s55, s73, 0
	v_mov_b32_e32 v3, v0
	global_load_dwordx4 v[4:7], v3, s[54:55]
	v_add_u32_e32 v3, 0x2000, v3
	global_load_dwordx4 v[8:11], v3, s[54:55]
	v_add_u32_e32 v3, 0x2000, v3
	s_waitcnt vmcnt(0)
	v_readlane_b32 s2, v254, 0
	v_readlane_b32 s3, v254, 1
	s_mov_b32 s70, s43
	v_mov_b32_e32 v0, v235
	v_readlane_b32 s0, v254, 6
	s_cmpk_lt_i32 s70, 0x100
	s_nop 0
	v_lshl_add_u32 v242, s0, 6, v218
	v_mov_b32_e32 v6, v242
	s_cselect_b64 s[6:7], -1, 0
	s_cmpk_gt_i32 s70, 0xff
	v_readfirstlane_b32 s0, v6
	s_cbranch_scc1 .LBB0_3303
	s_ashr_i32 s4, s70, 31
	s_lshr_b32 s4, s4, 29
	s_add_i32 s8, s70, s4
	s_and_b32 s4, s8, -8
	s_sub_i32 s9, s70, s4
	s_cmp_gt_i32 s9, -1
	s_mov_b64 s[4:5], -1
	s_cbranch_scc0 .LBB0_3300
	s_lshl_b32 s10, s9, 5
	s_mov_b64 s[4:5], 0

.LBB0_3841:
	v_readlane_b32 s2, v254, 0
	v_readlane_b32 s3, v254, 1
	s_load_dword s0, s[2:3], 0x128
	v_readlane_b32 s4, v254, 50
	s_add_i32 s29, s4, 5
	s_lshl_b32 s28, s48, 22
	s_waitcnt lgkmcnt(0)
	s_cmp_le_i32 s0, s29
	s_cbranch_scc0 .LBB0_3878
	s_load_dword s0, s[2:3], 0x12c
	s_waitcnt lgkmcnt(0)
	s_cmp_ge_i32 s29, s0
	s_cbranch_scc1 .LBB0_3878
	v_readlane_b32 s12, v254, 0
	v_readlane_b32 s13, v254, 1
	s_load_dwordx2 s[72:73], s[12:13], 0x120
	v_lshlrev_b32_e32 v0, 4, v235
	s_waitcnt lgkmcnt(0)
	s_mul_i32 s12, s48, 0x800000
	s_mul_i32 s13, s43, 0x8000
	s_add_u32 s12, s12, s13
	s_add_u32 s12, s12, 0x5900000
	s_add_u32 s54, s72, s12
	s_addc_u32 s55, s73, 0
	v_mov_b32_e32 v3, v0
	global_load_dwordx4 v[4:7], v3, s[54:55]
	v_add_u32_e32 v3, 0x2000, v3
	global_load_dwordx4 v[8:11], v3, s[54:55]
	v_add_u32_e32 v3, 0x2000, v3
	global_load_dwordx4 v[12:15], v3, s[54:55]
	v_add_u32_e32 v3, 0x2000, v3
	global_load_dwordx4 v[16:19], v3, s[54:55]
	v_add_u32_e32 v3, 0x2000, v3
	s_waitcnt vmcnt(0)
	v_readlane_b32 s2, v254, 0
	v_readlane_b32 s3, v254, 1
	s_mov_b32 s30, s43
	v_mov_b32_e32 v0, v235
	v_readlane_b32 s0, v254, 6
	s_cmpk_gt_i32 s30, 0x1ff
	s_nop 0
	v_lshl_add_u32 v6, s0, 6, v218
	s_nop 0
	v_readfirstlane_b32 s14, v6
	s_cbranch_scc1 .LBB0_3878
	s_ashr_i32 s31, s30, 31
	s_lshr_b32 s0, s31, 29
	s_add_i32 s9, s30, s0
	s_and_b32 s0, s9, -8
	s_sub_i32 s8, s30, s0
	s_cmp_gt_i32 s8, -1
	s_mov_b64 s[6:7], -1
	s_cbranch_scc0 .LBB0_3846
	s_lshl_b32 s0, s8, 6
	s_mov_b64 s[6:7], 0

.LBB0_3932:
	v_readlane_b32 s2, v254, 0
	v_readlane_b32 s3, v254, 1
	s_load_dword s0, s[2:3], 0x128
	v_readlane_b32 s4, v254, 50
	s_add_i32 s29, s4, 6
	s_waitcnt lgkmcnt(0)
	s_cmp_le_i32 s0, s29
	s_cbranch_scc0 .LBB0_3979
	s_load_dword s0, s[2:3], 0x12c
	s_waitcnt lgkmcnt(0)
	s_cmp_ge_i32 s29, s0
	s_cbranch_scc1 .LBB0_3979
	v_readlane_b32 s12, v254, 0
	v_readlane_b32 s13, v254, 1
	s_load_dwordx2 s[72:73], s[12:13], 0x120
	v_lshlrev_b32_e32 v0, 4, v235
	s_waitcnt lgkmcnt(0)
	s_mul_i32 s12, s48, 0x400000
	s_mul_i32 s13, s43, 0x4000
	s_add_u32 s12, s12, s13
	s_add_u32 s12, s12, 0x6900000
	s_add_u32 s54, s72, s12
	s_addc_u32 s55, s73, 0
	v_mov_b32_e32 v3, v0
	global_load_dwordx4 v[4:7], v3, s[54:55]
	v_add_u32_e32 v3, 0x2000, v3
	global_load_dwordx4 v[8:11], v3, s[54:55]
	v_add_u32_e32 v3, 0x2000, v3
	s_waitcnt vmcnt(0)
	v_readlane_b32 s2, v254, 0
	v_readlane_b32 s3, v254, 1
	s_mov_b32 s30, s43
	v_mov_b32_e32 v0, v235
	v_readlane_b32 s0, v254, 6
	s_cmpk_lt_i32 s30, 0x200
	s_nop 0
	v_lshl_add_u32 v6, s0, 6, v218
	s_cselect_b64 s[4:5], -1, 0
	s_cmpk_gt_i32 s30, 0x1ff
	v_readfirstlane_b32 s0, v6
	s_cbranch_scc1 .LBB0_3940
	s_ashr_i32 s6, s30, 31
	s_lshr_b32 s6, s6, 29
	s_add_i32 s8, s30, s6
	s_and_b32 s6, s8, -8
	s_sub_i32 s9, s30, s6
	s_cmp_gt_i32 s9, -1
	s_mov_b64 s[6:7], -1
	s_cbranch_scc0 .LBB0_3937
	s_lshl_b32 s10, s9, 6
	s_mov_b64 s[6:7], 0

.LBB0_4033:
	v_readlane_b32 s2, v254, 0
	v_readlane_b32 s3, v254, 1
	s_load_dword s0, s[2:3], 0x128
	v_readlane_b32 s4, v254, 50
	s_add_i32 s24, s4, 8
	s_waitcnt lgkmcnt(0)
	s_cmp_le_i32 s0, s24
	s_cbranch_scc0 .LBB0_4887
	s_load_dword s0, s[2:3], 0x12c
	s_waitcnt lgkmcnt(0)
	s_cmp_ge_i32 s24, s0
	s_cbranch_scc1 .LBB0_4887
	v_readlane_b32 s12, v254, 0
	v_readlane_b32 s13, v254, 1
	s_load_dwordx2 s[72:73], s[12:13], 0x120
	v_lshlrev_b32_e32 v0, 4, v235
	s_waitcnt lgkmcnt(0)
	s_mul_i32 s12, s48, 0x600000
	s_mul_i32 s13, s43, 0x6000
	s_add_u32 s12, s12, s13
	s_add_u32 s12, s12, 0x7900000
	s_add_u32 s54, s72, s12
	s_addc_u32 s55, s73, 0
	v_mov_b32_e32 v3, v0
	global_load_dwordx4 v[4:7], v3, s[54:55]
	v_add_u32_e32 v3, 0x2000, v3
	global_load_dwordx4 v[8:11], v3, s[54:55]
	v_add_u32_e32 v3, 0x2000, v3
	global_load_dwordx4 v[12:15], v3, s[54:55]
	v_add_u32_e32 v3, 0x2000, v3
	s_waitcnt vmcnt(0)
	v_readlane_b32 s10, v254, 0
	v_readlane_b32 s11, v254, 1
	s_load_dwordx2 s[8:9], s[10:11], 0x120
	s_mov_b32 s25, s43
	s_cmpk_gt_i32 s25, 0x9f
	v_readlane_b32 s4, v254, 31
	s_cselect_b64 s[2:3], -1, 0
	v_readlane_b32 s5, v254, 32
	s_and_b64 s[2:3], s[4:5], s[2:3]
	s_waitcnt vmcnt(0)
	v_mov_b32_e32 v161, v235
	v_readlane_b32 s26, v254, 6
	s_andn2_b64 vcc, exec, s[2:3]
	s_cbranch_vccnz .LBB0_4850
	v_cmp_eq_u32_e32 vcc, 0, v161
	s_and_saveexec_b64 s[2:3], vcc
	s_cbranch_execz .LBB0_4040
	s_mov_b64 s[6:7], exec
	v_mbcnt_lo_u32_b32 v0, s6, 0
	v_mbcnt_hi_u32_b32 v0, s7, v0
	v_cmp_eq_u32_e32 vcc, 0, v0
	s_and_saveexec_b64 s[4:5], vcc
	s_cbranch_execz .LBB0_4039
	s_bcnt1_i32_b64 s0, s[6:7]
	s_mulk_i32 s0, 0x90
	v_mov_b32_e32 v2, s0
	v_mov_b32_e32 v3, 0x38000
	s_waitcnt lgkmcnt(0)
	global_atomic_add v2, v3, v2, s[8:9] sc0

.LBB0_5016:
	v_readlane_b32 s2, v254, 0
	v_readlane_b32 s3, v254, 1
	s_load_dword s0, s[2:3], 0x128
	v_readlane_b32 s4, v254, 50
	s_add_i32 s30, s4, 10
	s_waitcnt lgkmcnt(0)
	s_cmp_le_i32 s0, s30
	s_cbranch_scc0 .LBB0_5063
	s_load_dword s0, s[2:3], 0x12c
	s_waitcnt lgkmcnt(0)
	s_cmp_ge_i32 s30, s0
	s_cbranch_scc1 .LBB0_5063
	v_readlane_b32 s12, v254, 0
	v_readlane_b32 s13, v254, 1
	s_load_dwordx2 s[72:73], s[12:13], 0x120
	v_lshlrev_b32_e32 v0, 4, v235
	s_waitcnt lgkmcnt(0)
	s_mul_i32 s12, s48, 0x200000
	s_mul_i32 s13, s43, 0x2000
	s_add_u32 s12, s12, s13
	s_add_u32 s12, s12, 0x8500000
	s_add_u32 s54, s72, s12
	s_addc_u32 s55, s73, 0
	v_mov_b32_e32 v3, v0
	global_load_dwordx4 v[4:7], v3, s[54:55]
	v_add_u32_e32 v3, 0x2000, v3
	s_waitcnt vmcnt(0)
	v_readlane_b32 s2, v254, 0
	v_readlane_b32 s3, v254, 1
	s_mov_b32 s31, s43
	v_mov_b32_e32 v0, v235
	v_readlane_b32 s0, v254, 6
	s_cmpk_lt_i32 s31, 0x200
	s_nop 0
	v_lshl_add_u32 v6, s0, 6, v218
	s_cselect_b64 s[4:5], -1, 0
	s_cmpk_gt_i32 s31, 0x1ff
	v_readfirstlane_b32 s0, v6
	s_cbranch_scc1 .LBB0_5024
	s_ashr_i32 s6, s31, 31
	s_lshr_b32 s6, s6, 29
	s_add_i32 s8, s31, s6
	s_and_b32 s6, s8, -8
	s_sub_i32 s9, s31, s6
	s_cmp_gt_i32 s9, -1
	s_mov_b64 s[6:7], -1
	s_cbranch_scc0 .LBB0_5021
	s_lshl_b32 s10, s9, 6
	s_mov_b64 s[6:7], 0
